# expert-weight conversion loop: counted waits no longer drain the previous tile's stores (vmcnt 20 / 4); split re-tuned to 96 converter workgroups, 96 tiles kept in phase 1
# baseline (speedup 1.0000x reference)
.LBB0_364:
	v_and_b32_e32 v2, 0xfc, v200
	v_lshrrev_b32_e32 v141, 6, v0
	s_cmpk_gt_i32 s12, 0x5f
	v_mov_b32_e32 v135, 0
	v_lshlrev_b32_e32 v136, 2, v2
	s_cbranch_scc1 .LBB0_366
	s_mul_hi_i32 s0, s12, 0x92492493
	s_add_i32 s0, s0, s12
	s_lshr_b32 s1, s0, 31
	s_ashr_i32 s0, s0, 11
	s_add_i32 s10, s0, s1
	s_mul_i32 s0, s10, 0xfffff200
	s_add_i32 s0, s0, s12
	s_mul_hi_i32 s1, s0, 0x92492493
	s_add_i32 s1, s1, s0
	s_lshr_b32 s2, s1, 31
	s_ashr_i32 s1, s1, 8
	s_add_i32 s8, s1, s2
	s_mul_i32 s1, s8, 0xfffffe40
	s_add_i32 s4, s1, s0
	s_mul_i32 s6, s8, 0x3800000
	s_mul_hi_i32 s5, s8, 0x3800000
	s_add_u32 s7, s52, s6
	s_addc_u32 s9, s53, s5
	s_lshl_b32 s0, s4, 4
	s_and_b32 s0, s0, 0xffffff80
	s_ashr_i32 s1, s0, 31
	s_lshl_b64 s[2:3], s[0:1], 13
	s_add_u32 s1, s7, s2
	s_addc_u32 s2, s9, s3
	s_lshl_b32 s3, s12, 8
	s_and_b32 s11, s3, 0x700
	s_lshl_b32 s7, s11, 2
	s_add_u32 s1, s1, s7
	s_addc_u32 s2, s2, 0
	s_mul_i32 s9, s8, 0xe00000
	s_mul_hi_i32 s7, s8, 0xe00000
	s_add_u32 s14, s88, s9
	s_addc_u32 s15, s89, s7
	s_mul_hi_i32 s7, s4, 0x92492493
	s_add_i32 s7, s7, s4
	s_lshr_b32 s9, s7, 31
	s_ashr_i32 s7, s7, 4
	s_add_i32 s7, s7, s9
	s_mul_i32 s9, s7, 0xffffffe4
	s_add_i32 s9, s9, s4
	s_add_i32 s4, s12, 0xdff
	v_readlane_b32 s16, v251, 0
	s_cmpk_lt_u32 s4, 0x1bff
	v_readlane_b32 s20, v251, 4
	v_readlane_b32 s22, v251, 6
	v_readlane_b32 s21, v251, 5
	v_readlane_b32 s23, v251, 7
	s_cselect_b32 s16, s20, s22
	s_cselect_b32 s4, s21, s23
	s_add_u32 s6, s16, s6
	v_readlane_b32 s17, v251, 1
	s_addc_u32 s4, s4, s5
	s_lshl_b32 s16, s7, 7
	s_mul_i32 s7, s7, 0x380000
	v_readlane_b32 s18, v251, 2
	s_mul_hi_i32 s5, s16, 0x7000
	s_add_u32 s17, s6, s7
	s_addc_u32 s18, s4, s5
	s_lshl_b32 s4, s9, 8
	s_ashr_i32 s5, s4, 31
	s_lshl_b64 s[6:7], s[4:5], 2
	s_add_u32 s5, s17, s6
	s_addc_u32 s6, s18, s7
	s_mul_hi_i32 s7, s8, 0x1c00000
	s_mul_i32 s8, s8, 0x1c00000
	s_add_u32 s17, s90, s8
	s_addc_u32 s7, s91, s7
	s_cmpk_lt_i32 s12, 0x1c00
	s_cselect_b32 s8, s5, s1
	s_movk_i32 s1, 0x800
	s_cselect_b32 s1, 0x1c00, s1
	v_mul_u32_u24_e32 v2, s1, v141
	s_cselect_b32 s9, s6, s2
	v_lshlrev_b32_e32 v134, 2, v2
	v_lshl_add_u64 v[2:3], s[8:9], 0, v[134:135]
	v_mov_b32_e32 v137, v135
	s_mov_b32 s3, 0
	s_cselect_b32 s10, s10, 2
	s_cselect_b32 s4, s4, s11
	s_cselect_b32 s0, s16, s0
	s_cselect_b32 s7, s7, s15
	s_cselect_b32 s6, s17, s14
	v_lshl_add_u64 v[2:3], v[2:3], 0, v[136:137]
	s_lshl_b32 s2, s1, 5
	s_waitcnt vmcnt(0)
	v_lshl_add_u64 v[10:11], v[2:3], 0, s[2:3]
	global_load_dwordx4 v[2:5], v[2:3], off nt
	s_waitcnt lgkmcnt(0)
	global_load_dwordx4 v[6:9], v[10:11], off nt
	v_lshl_add_u64 v[10:11], v[10:11], 0, s[2:3]
	v_lshl_add_u64 v[18:19], v[10:11], 0, s[2:3]
	global_load_dwordx4 v[10:13], v[10:11], off nt
	s_nop 0
	global_load_dwordx4 v[14:17], v[18:19], off nt
	v_lshl_add_u64 v[18:19], v[18:19], 0, s[2:3]
	v_lshl_add_u64 v[26:27], v[18:19], 0, s[2:3]
	global_load_dwordx4 v[18:21], v[18:19], off nt
	s_nop 0
	global_load_dwordx4 v[22:25], v[26:27], off nt
	v_lshl_add_u64 v[26:27], v[26:27], 0, s[2:3]
	v_lshl_add_u64 v[34:35], v[26:27], 0, s[2:3]
	v_lshl_add_u64 v[38:39], v[34:35], 0, s[2:3]
	v_lshl_add_u64 v[42:43], v[38:39], 0, s[2:3]
	v_lshl_add_u64 v[46:47], v[42:43], 0, s[2:3]
	v_lshl_add_u64 v[50:51], v[46:47], 0, s[2:3]
	v_lshl_add_u64 v[54:55], v[50:51], 0, s[2:3]
	v_lshl_add_u64 v[58:59], v[54:55], 0, s[2:3]
	v_lshl_add_u64 v[62:63], v[58:59], 0, s[2:3]
	global_load_dwordx4 v[26:29], v[26:27], off nt
	s_nop 0
	global_load_dwordx4 v[30:33], v[34:35], off nt
	v_readlane_b32 s19, v251, 3
	global_load_dwordx4 v[34:37], v[38:39], off nt
	s_nop 0
	global_load_dwordx4 v[38:41], v[42:43], off nt
	s_nop 0
	global_load_dwordx4 v[42:45], v[46:47], off nt
	s_nop 0
	global_load_dwordx4 v[46:49], v[50:51], off nt
	s_nop 0
	global_load_dwordx4 v[50:53], v[54:55], off nt
	s_nop 0
	global_load_dwordx4 v[54:57], v[58:59], off nt
	s_nop 0
	global_load_dwordx4 v[58:61], v[62:63], off nt
	v_lshl_add_u64 v[62:63], v[62:63], 0, s[2:3]
	global_load_dwordx4 v[62:65], v[62:63], off nt
	s_branch .LBB0_367

.LBB0_370:
	s_cmpk_gt_i32 s18, 0x5f
	s_mov_b64 s[42:43], -1
	s_cbranch_scc1 .LBB0_369
	s_add_i32 s18, s18, s13
	s_cmpk_lt_i32 s18, 0x60
	s_cselect_b64 s[44:45], -1, 0
	s_cmpk_gt_i32 s18, 0x5f
	s_cselect_b64 s[42:43], -1, 0
	s_and_b64 vcc, exec, s[42:43]
	s_cbranch_vccnz .LBB0_378
	s_mul_hi_i32 s1, s18, 0x92492493
	s_add_i32 s1, s1, s18
	s_lshr_b32 s2, s1, 31
	s_ashr_i32 s1, s1, 11
	s_add_i32 s17, s1, s2
	s_mul_i32 s1, s17, 0xfffff200
	s_add_i32 s2, s1, s18
	s_mul_hi_i32 s1, s2, 0x92492493
	s_add_i32 s1, s1, s2
	s_lshr_b32 s3, s1, 31
	s_ashr_i32 s1, s1, 8
	s_add_i32 s1, s1, s3
	s_mul_i32 s19, s1, 0xfffffe40
	s_add_i32 s19, s19, s2
	s_mov_b64 s[46:47], -1
	s_cmpk_gt_i32 s18, 0x1bff
	s_mul_hi_i32 s5, s1, 0x3800000
	s_mul_i32 s8, s1, 0x3800000
	s_cbranch_scc0 .LBB0_374
	s_add_u32 s20, s52, s8
	s_addc_u32 s21, s53, s5
	s_lshl_b32 s2, s19, 4
	s_and_b32 s14, s2, 0xffffff80
	s_ashr_i32 s15, s14, 31
	s_lshl_b64 s[2:3], s[14:15], 13
	s_add_u32 s2, s20, s2
	s_addc_u32 s3, s21, s3
	s_lshl_b32 s15, s18, 8
	s_and_b32 s36, s15, 0x700
	s_lshl_b32 s15, s36, 2
	s_add_u32 s2, s2, s15
	s_addc_u32 s3, s3, 0
	s_mul_i32 s20, s1, 0xe00000
	s_mul_hi_i32 s15, s1, 0xe00000
	s_add_u32 s40, s88, s20
	s_addc_u32 s41, s89, s15
	s_mov_b64 s[46:47], 0

.LBB0_394:
	s_andn2_b64 vcc, exec, s[44:45]
	s_waitcnt lgkmcnt(0)
	s_barrier
	s_cbranch_vccnz .LBB0_369
	s_add_i32 s18, s18, s13
	s_cmpk_gt_i32 s18, 0x5f
	s_cbranch_scc1 .LBB0_402
	s_mul_hi_i32 s0, s18, 0x92492493
	s_add_i32 s0, s0, s18
	s_lshr_b32 s1, s0, 31
	s_ashr_i32 s0, s0, 11
	s_add_i32 s10, s0, s1
	s_mul_i32 s0, s10, 0xfffff200
	s_add_i32 s0, s0, s18
	s_mul_hi_i32 s1, s0, 0x92492493
	s_add_i32 s1, s1, s0
	s_lshr_b32 s2, s1, 31
	s_ashr_i32 s8, s1, 8
	s_add_i32 s8, s8, s2
	s_mul_i32 s19, s8, 0xfffffe40
	s_add_i32 s19, s19, s0
	s_mov_b64 s[44:45], -1
	s_cmpk_gt_i32 s18, 0x1bff
	s_mul_hi_i32 s5, s8, 0x3800000
	s_mul_i32 s15, s8, 0x3800000
	s_cbranch_scc0 .LBB0_398
	s_add_u32 s4, s52, s15
	s_addc_u32 s6, s53, s5
	s_lshl_b32 s0, s19, 4
	s_and_b32 s0, s0, 0xffffff80
	s_ashr_i32 s1, s0, 31
	s_lshl_b64 s[2:3], s[0:1], 13
	s_add_u32 s1, s4, s2
	s_addc_u32 s3, s6, s3
	s_lshl_b32 s2, s18, 8
	s_and_b32 s4, s2, 0x700
	s_lshl_b32 s2, s4, 2
	s_add_u32 s2, s1, s2
	s_addc_u32 s3, s3, 0
	s_mul_i32 s6, s8, 0xe00000
	s_mul_hi_i32 s1, s8, 0xe00000
	s_add_u32 s6, s88, s6
	s_addc_u32 s7, s89, s1
	s_mov_b64 s[44:45], 0

.LBB0_839:
	s_add_u32 s16, s56, 0x3eb00000
	s_addc_u32 s17, s57, 0
	s_cmp_lt_i32 s58, 8
	s_cselect_b64 s[0:1], -1, 0
	s_cmp_gt_i32 s59, 7
	s_cselect_b64 s[2:3], -1, 0
	s_and_b64 s[0:1], s[0:1], s[2:3]
	s_andn2_b64 vcc, exec, s[0:1]
	s_cbranch_vccnz .LBB0_921
	s_mov_b32 s99, s13
	s_cmp_lt_u32 s12, 160
	s_cbranch_scc1 .Lsp7_gemm
	s_mov_b32 s98, s12
	s_add_i32 s12, s12, -64
	s_mov_b32 s13, 96
	v_lshrrev_b32_e32 v140, 3, v0
	s_add_u32 s0, s94, 0xffffffe0
	s_addc_u32 s1, s95, -1
	s_load_dwordx2 s[52:53], s[0:1], 0x0
	s_waitcnt lgkmcnt(0)
	s_branch .Lcv_364
